# MoE unit scheduler search via one LDS read + popcount; packed-f32 SwiGLU epilogue; earlier wait fixes
# speedup vs baseline: 1.0296x; 1.0296x over previous
;     __device__ __forceinline__ bool next(int i, Unit& u) const {
;         const int L = i * G + c; if (L >= total) return false;
;         int e = 0;
; #pragma unroll 1
;         for (int j = 1; j < NEXP; ++j) e = (L >= pre[j]) ? j : e;
;         const int rem = L - pre[e];
;         u.e = e; u.pn = rem % NT; u.mt = rem / NT; u.pm = 0; return true;
;     }
.LBB0_3129:
	s_add_i32 s37, s37, 1
	s_mul_i32 s31, s37, s68
	v_readlane_b32 s35, v250, 39
	s_add_i32 s31, s31, s35
	v_cmp_ge_i32_e32 vcc, s31, v1
	v_cmp_lt_i32_e64 s[40:41], s31, v1
	s_cbranch_vccnz .LBB0_3135
	v_lshl_add_u32 v2, v195, 2, 0
	v_add_u32_e32 v2, 0x23100, v2
	ds_read_b32 v2, v2
	s_waitcnt lgkmcnt(0)
	v_cmp_ge_i32_e32 vcc, s31, v2
	s_and_b32 s30, vcc_lo, -2
	s_bcnt1_i32_b32 s30, s30
	s_nop 3
	v_readlane_b32 s34, v2, s30
	s_sub_i32 s31, s31, s34
	s_ashr_i32 s34, s31, 31
	s_lshr_b32 s34, s34, 29
	s_add_i32 s34, s31, s34
	s_ashr_i32 s45, s34, 3
	s_and_b32 s34, s34, -8
	s_sub_i32 s34, s31, s34

; __device__ __forceinline__ unsigned pk4_fp8(float a, float b, float c, float d) { int r = __builtin_amdgcn_cvt_pk_fp8_f32(a, b, 0, false); return (unsigned)__builtin_amdgcn_cvt_pk_fp8_f32(c, d, r, true); }
;     __device__ __forceinline__ void operator()(const f32x4 (&acc)[2][2][4][2], const Unit& u, int wr, int wc, int fr, int fq) const {
;         const int r0 = rowoff[u.e] + u.mt * BM + wr * 64 + fr, j0 = u.pn * HALF + wc * 32 + 8 * fq;
;         f32x4 gb[2], ub[2];
; #pragma unroll
;         for (int n = 0; n < 2; ++n) { gb[n] = *(const f32x4*)(bg + u.e * 1024 + j0 + 4 * n); ub[n] = *(const f32x4*)(bu + u.e * 1024 + j0 + 4 * n); }
; #pragma unroll
;         for (int ai = 0; ai < 2; ++ai)
; #pragma unroll
;             for (int m = 0; m < 4; ++m) { unsigned char* rowp = (unsigned char*)H + (size_t)(r0 + ai * HALF + m * 16) * 1024 + j0; float hv[8];
; #pragma unroll
;                 for (int n = 0; n < 2; ++n)
; #pragma unroll
;                     for (int j = 0; j < 4; ++j) { float g = acc[ai][0][m][n][j] * ws + gb[n][j], up = acc[ai][1][m][n][j] * ws + ub[n][j];
;                         g = fminf(g, 7.f); up = fminf(fmaxf(up, -7.f), 7.f);
;                         hv[n * 4 + j] = (up + 1.f) * g * __builtin_amdgcn_rcpf(1.f + __expf(-1.702f * g)); }
;                 *(u32x2*)rowp = (u32x2){pk4_fp8(4.f * hv[0], 4.f * hv[1], 4.f * hv[2], 4.f * hv[3]), pk4_fp8(4.f * hv[4], 4.f * hv[5], 4.f * hv[6], 4.f * hv[7])}; }
;     }
.LBB0_3151:
	s_lshl_b32 s31, s42, 2
	s_add_i32 s31, s31, 0
	s_lshl_b32 s42, s42, 10
	s_add_i32 s31, s31, 0x23240
	s_ashr_i32 s43, s42, 31
	v_mov_b32_e32 v2, s31
	s_lshl_b32 s31, s52, 8
	s_lshl_b64 s[42:43], s[42:43], 2
	s_add_u32 s46, s19, s42
	v_lshl_or_b32 v18, s44, 7, v175
	s_addc_u32 s47, s20, s43
	v_ashrrev_i32_e32 v19, 31, v18
	s_add_u32 s42, s21, s42
	ds_read_b32 v20, v2
	v_lshlrev_b64 v[2:3], 2, v[18:19]
	s_addc_u32 s43, s22, s43
	v_lshl_add_u64 v[6:7], s[46:47], 0, v[2:3]
	v_lshl_add_u64 v[14:15], s[42:43], 0, v[2:3]
	global_load_dwordx4 v[2:5], v[6:7], off offset:16
	global_load_dwordx4 v[10:13], v[6:7], off
	s_nop 0
	global_load_dwordx4 v[6:9], v[14:15], off offset:16
	s_nop 0
	global_load_dwordx4 v[14:17], v[14:15], off
	s_mov_b32 s35, 0xc0e00000
	s_waitcnt lgkmcnt(0)
	v_add_u32_e32 v20, s31, v20
	v_add_u32_e32 v20, v20, v206
	v_ashrrev_i32_e32 v21, 31, v20
	v_lshlrev_b64 v[20:21], 10, v[20:21]
	v_lshl_add_u64 v[20:21], s[14:15], 0, v[20:21]
	v_lshl_add_u64 v[18:19], v[20:21], 0, v[18:19]
	v_mov_b32_e32 v20, v35
	s_movk_i32 s31, 0x4000
	s_mov_b64 s[42:43], -1
	s_mov_b64 s[76:77], 0x30080
	s_mov_b32 s84, s78
	s_mov_b64 s[86:87], s[88:89]
	s_waitcnt vmcnt(0)
	v_mov_b32_e32 v24, 0x3c000000
	v_mov_b32_e32 v25, 0x3c000000
	v_mov_b32_e32 v26, 0xbfd9db23
	v_mov_b32_e32 v27, 0xbfd9db23
	s_mov_b32 s51, 0
	v_pk_fma_f32 v[160:161], v[160:161], v[24:25], v[10:11]
	v_pk_fma_f32 v[162:163], v[162:163], v[24:25], v[12:13]
	v_pk_fma_f32 v[152:153], v[152:153], v[24:25], v[2:3]
	v_pk_fma_f32 v[154:155], v[154:155], v[24:25], v[4:5]
	v_pk_fma_f32 v[156:157], v[156:157], v[24:25], v[14:15]
	v_pk_fma_f32 v[158:159], v[158:159], v[24:25], v[16:17]
	v_pk_fma_f32 v[148:149], v[148:149], v[24:25], v[6:7]
	v_pk_fma_f32 v[150:151], v[150:151], v[24:25], v[8:9]
	v_min_f32_e32 v160, 0x40e00000, v160
	v_min_f32_e32 v161, 0x40e00000, v161
	v_min_f32_e32 v162, 0x40e00000, v162
	v_min_f32_e32 v163, 0x40e00000, v163
	v_min_f32_e32 v152, 0x40e00000, v152
	v_min_f32_e32 v153, 0x40e00000, v153
	v_min_f32_e32 v154, 0x40e00000, v154
	v_min_f32_e32 v155, 0x40e00000, v155
	v_med3_f32 v156, v156, s35, v200
	v_med3_f32 v157, v157, s35, v200
	v_med3_f32 v158, v158, s35, v200
	v_med3_f32 v159, v159, s35, v200
	v_med3_f32 v148, v148, s35, v200
	v_med3_f32 v149, v149, s35, v200
	v_med3_f32 v150, v150, s35, v200
	v_med3_f32 v151, v151, s35, v200
	v_pk_add_f32 v[156:157], v[156:157], 1.0 op_sel_hi:[1,0]
	v_pk_add_f32 v[158:159], v[158:159], 1.0 op_sel_hi:[1,0]
	v_pk_add_f32 v[148:149], v[148:149], 1.0 op_sel_hi:[1,0]
	v_pk_add_f32 v[150:151], v[150:151], 1.0 op_sel_hi:[1,0]
	v_pk_mul_f32 v[156:157], v[160:161], v[156:157]
	v_pk_mul_f32 v[158:159], v[162:163], v[158:159]
	v_pk_mul_f32 v[148:149], v[152:153], v[148:149]
	v_pk_mul_f32 v[150:151], v[154:155], v[150:151]
	v_pk_mul_f32 v[160:161], v[160:161], v[26:27]
	v_pk_mul_f32 v[162:163], v[162:163], v[26:27]
	v_pk_mul_f32 v[152:153], v[152:153], v[26:27]
	v_pk_mul_f32 v[154:155], v[154:155], v[26:27]
	v_pk_mul_f32 v[160:161], v[160:161], v[196:197] op_sel_hi:[1,0]
	v_pk_mul_f32 v[162:163], v[162:163], v[196:197] op_sel_hi:[1,0]
	v_pk_mul_f32 v[152:153], v[152:153], v[196:197] op_sel_hi:[1,0]
	v_pk_mul_f32 v[154:155], v[154:155], v[196:197] op_sel_hi:[1,0]
	v_exp_f32_e32 v160, v160
	v_exp_f32_e32 v161, v161
	v_exp_f32_e32 v162, v162
	v_exp_f32_e32 v163, v163
	v_exp_f32_e32 v152, v152
	v_exp_f32_e32 v153, v153
	v_exp_f32_e32 v154, v154
	v_exp_f32_e32 v155, v155
	v_pk_add_f32 v[160:161], v[160:161], 1.0 op_sel_hi:[1,0]
	v_pk_add_f32 v[162:163], v[162:163], 1.0 op_sel_hi:[1,0]
	v_pk_add_f32 v[152:153], v[152:153], 1.0 op_sel_hi:[1,0]
	v_pk_add_f32 v[154:155], v[154:155], 1.0 op_sel_hi:[1,0]
	v_rcp_f32_e32 v160, v160
	v_rcp_f32_e32 v161, v161
	v_rcp_f32_e32 v162, v162
	v_rcp_f32_e32 v163, v163
	v_rcp_f32_e32 v152, v152
	v_rcp_f32_e32 v153, v153
	v_rcp_f32_e32 v154, v154
	v_rcp_f32_e32 v155, v155
	v_pk_mul_f32 v[156:157], v[156:157], v[160:161]
	v_pk_mul_f32 v[158:159], v[158:159], v[162:163]
	v_pk_mul_f32 v[148:149], v[148:149], v[152:153]
	v_pk_mul_f32 v[150:151], v[150:151], v[154:155]
	v_pk_mul_f32 v[156:157], v[156:157], 4.0 op_sel_hi:[1,0]
	v_pk_mul_f32 v[158:159], v[158:159], 4.0 op_sel_hi:[1,0]
	v_pk_mul_f32 v[148:149], v[148:149], 4.0 op_sel_hi:[1,0]
	v_pk_mul_f32 v[150:151], v[150:151], 4.0 op_sel_hi:[1,0]
	v_cvt_pk_fp8_f32 v20, v156, v157
	v_cvt_pk_fp8_f32 v21, v148, v149
	s_nop 0
	v_cvt_pk_fp8_f32 v20, v158, v159 op_sel:[0,0,1]
	v_cvt_pk_fp8_f32 v21, v150, v151 op_sel:[0,0,1]
	s_nop 0
	global_store_dwordx2 v[18:19], v[20:21], off
	v_pk_fma_f32 v[144:145], v[144:145], v[24:25], v[10:11]
	v_pk_fma_f32 v[146:147], v[146:147], v[24:25], v[12:13]
	v_pk_fma_f32 v[136:137], v[136:137], v[24:25], v[2:3]
	v_pk_fma_f32 v[138:139], v[138:139], v[24:25], v[4:5]
	v_pk_fma_f32 v[140:141], v[140:141], v[24:25], v[14:15]
	v_pk_fma_f32 v[142:143], v[142:143], v[24:25], v[16:17]
	v_pk_fma_f32 v[132:133], v[132:133], v[24:25], v[6:7]
	v_pk_fma_f32 v[134:135], v[134:135], v[24:25], v[8:9]
	v_min_f32_e32 v144, 0x40e00000, v144
	v_min_f32_e32 v145, 0x40e00000, v145
	v_min_f32_e32 v146, 0x40e00000, v146
	v_min_f32_e32 v147, 0x40e00000, v147
	v_min_f32_e32 v136, 0x40e00000, v136
	v_min_f32_e32 v137, 0x40e00000, v137
	v_min_f32_e32 v138, 0x40e00000, v138
	v_min_f32_e32 v139, 0x40e00000, v139
	v_med3_f32 v140, v140, s35, v200
	v_med3_f32 v141, v141, s35, v200
	v_med3_f32 v142, v142, s35, v200
	v_med3_f32 v143, v143, s35, v200
	v_med3_f32 v132, v132, s35, v200
	v_med3_f32 v133, v133, s35, v200
	v_med3_f32 v134, v134, s35, v200
	v_med3_f32 v135, v135, s35, v200
	v_pk_add_f32 v[140:141], v[140:141], 1.0 op_sel_hi:[1,0]
; __device__ __forceinline__ unsigned pk4_fp8(float a, float b, float c, float d) { int r = __builtin_amdgcn_cvt_pk_fp8_f32(a, b, 0, false); return (unsigned)__builtin_amdgcn_cvt_pk_fp8_f32(c, d, r, true); }
;     __device__ __forceinline__ void operator()(const f32x4 (&acc)[2][2][4][2], const Unit& u, int wr, int wc, int fr, int fq) const {
;     ...
;                 for (int n = 0; n < 2; ++n)
; #pragma unroll
;                     for (int j = 0; j < 4; ++j) { float g = acc[ai][0][m][n][j] * ws + gb[n][j], up = acc[ai][1][m][n][j] * ws + ub[n][j];
;                         g = fminf(g, 7.f); up = fminf(fmaxf(up, -7.f), 7.f);
;                         hv[n * 4 + j] = (up + 1.f) * g * __builtin_amdgcn_rcpf(1.f + __expf(-1.702f * g)); }
;                 *(u32x2*)rowp = (u32x2){pk4_fp8(4.f * hv[0], 4.f * hv[1], 4.f * hv[2], 4.f * hv[3]), pk4_fp8(4.f * hv[4], 4.f * hv[5], 4.f * hv[6], 4.f * hv[7])}; }
	v_pk_add_f32 v[142:143], v[142:143], 1.0 op_sel_hi:[1,0]
	v_pk_add_f32 v[132:133], v[132:133], 1.0 op_sel_hi:[1,0]
	v_pk_add_f32 v[134:135], v[134:135], 1.0 op_sel_hi:[1,0]
	v_pk_mul_f32 v[140:141], v[144:145], v[140:141]
	v_pk_mul_f32 v[142:143], v[146:147], v[142:143]
	v_pk_mul_f32 v[132:133], v[136:137], v[132:133]
	v_pk_mul_f32 v[134:135], v[138:139], v[134:135]
	v_pk_mul_f32 v[144:145], v[144:145], v[26:27]
	v_pk_mul_f32 v[146:147], v[146:147], v[26:27]
	v_pk_mul_f32 v[136:137], v[136:137], v[26:27]
	v_pk_mul_f32 v[138:139], v[138:139], v[26:27]
	v_pk_mul_f32 v[144:145], v[144:145], v[196:197] op_sel_hi:[1,0]
	v_pk_mul_f32 v[146:147], v[146:147], v[196:197] op_sel_hi:[1,0]
	v_pk_mul_f32 v[136:137], v[136:137], v[196:197] op_sel_hi:[1,0]
	v_pk_mul_f32 v[138:139], v[138:139], v[196:197] op_sel_hi:[1,0]
	v_exp_f32_e32 v144, v144
	v_exp_f32_e32 v145, v145
	v_exp_f32_e32 v146, v146
	v_exp_f32_e32 v147, v147
	v_exp_f32_e32 v136, v136
	v_exp_f32_e32 v137, v137
	v_exp_f32_e32 v138, v138
	v_exp_f32_e32 v139, v139
	v_pk_add_f32 v[144:145], v[144:145], 1.0 op_sel_hi:[1,0]
	v_pk_add_f32 v[146:147], v[146:147], 1.0 op_sel_hi:[1,0]
	v_pk_add_f32 v[136:137], v[136:137], 1.0 op_sel_hi:[1,0]
	v_pk_add_f32 v[138:139], v[138:139], 1.0 op_sel_hi:[1,0]
	v_rcp_f32_e32 v144, v144
	v_rcp_f32_e32 v145, v145
	v_rcp_f32_e32 v146, v146
	v_rcp_f32_e32 v147, v147
	v_rcp_f32_e32 v136, v136
	v_rcp_f32_e32 v137, v137
	v_rcp_f32_e32 v138, v138
	v_rcp_f32_e32 v139, v139
	v_pk_mul_f32 v[140:141], v[140:141], v[144:145]
	v_pk_mul_f32 v[142:143], v[142:143], v[146:147]
	v_pk_mul_f32 v[132:133], v[132:133], v[136:137]
	v_pk_mul_f32 v[134:135], v[134:135], v[138:139]
	v_pk_mul_f32 v[140:141], v[140:141], 4.0 op_sel_hi:[1,0]
	v_pk_mul_f32 v[142:143], v[142:143], 4.0 op_sel_hi:[1,0]
	v_pk_mul_f32 v[132:133], v[132:133], 4.0 op_sel_hi:[1,0]
	v_pk_mul_f32 v[134:135], v[134:135], 4.0 op_sel_hi:[1,0]
	s_mov_b32 s50, 0x4000
	v_cvt_pk_fp8_f32 v20, v140, v141
	v_cvt_pk_fp8_f32 v21, v132, v133
	v_lshl_add_u64 v[22:23], s[50:51], 0, v[18:19]
	v_cvt_pk_fp8_f32 v20, v142, v143 op_sel:[0,0,1]
	v_cvt_pk_fp8_f32 v21, v134, v135 op_sel:[0,0,1]
	s_nop 0
	global_store_dwordx2 v[22:23], v[20:21], off
	v_pk_fma_f32 v[128:129], v[128:129], v[24:25], v[10:11]
	v_pk_fma_f32 v[130:131], v[130:131], v[24:25], v[12:13]
	v_pk_fma_f32 v[120:121], v[120:121], v[24:25], v[2:3]
	v_pk_fma_f32 v[122:123], v[122:123], v[24:25], v[4:5]
	v_pk_fma_f32 v[124:125], v[124:125], v[24:25], v[14:15]
	v_pk_fma_f32 v[126:127], v[126:127], v[24:25], v[16:17]
	v_pk_fma_f32 v[116:117], v[116:117], v[24:25], v[6:7]
	v_pk_fma_f32 v[118:119], v[118:119], v[24:25], v[8:9]
	v_min_f32_e32 v128, 0x40e00000, v128
	v_min_f32_e32 v129, 0x40e00000, v129
	v_min_f32_e32 v130, 0x40e00000, v130
	v_min_f32_e32 v131, 0x40e00000, v131
	v_min_f32_e32 v120, 0x40e00000, v120
	v_min_f32_e32 v121, 0x40e00000, v121
	v_min_f32_e32 v122, 0x40e00000, v122
	v_min_f32_e32 v123, 0x40e00000, v123
	v_med3_f32 v124, v124, s35, v200
	v_med3_f32 v125, v125, s35, v200
	v_med3_f32 v126, v126, s35, v200
	v_med3_f32 v127, v127, s35, v200
	v_med3_f32 v116, v116, s35, v200
	v_med3_f32 v117, v117, s35, v200
	v_med3_f32 v118, v118, s35, v200
	v_med3_f32 v119, v119, s35, v200
	v_pk_add_f32 v[124:125], v[124:125], 1.0 op_sel_hi:[1,0]
	v_pk_add_f32 v[126:127], v[126:127], 1.0 op_sel_hi:[1,0]
	v_pk_add_f32 v[116:117], v[116:117], 1.0 op_sel_hi:[1,0]
	v_pk_add_f32 v[118:119], v[118:119], 1.0 op_sel_hi:[1,0]
	v_pk_mul_f32 v[124:125], v[128:129], v[124:125]
	v_pk_mul_f32 v[126:127], v[130:131], v[126:127]
	v_pk_mul_f32 v[116:117], v[120:121], v[116:117]
	v_pk_mul_f32 v[118:119], v[122:123], v[118:119]
	v_pk_mul_f32 v[128:129], v[128:129], v[26:27]
	v_pk_mul_f32 v[130:131], v[130:131], v[26:27]
	v_pk_mul_f32 v[120:121], v[120:121], v[26:27]
	v_pk_mul_f32 v[122:123], v[122:123], v[26:27]
	v_pk_mul_f32 v[128:129], v[128:129], v[196:197] op_sel_hi:[1,0]
	v_pk_mul_f32 v[130:131], v[130:131], v[196:197] op_sel_hi:[1,0]
	v_pk_mul_f32 v[120:121], v[120:121], v[196:197] op_sel_hi:[1,0]
	v_pk_mul_f32 v[122:123], v[122:123], v[196:197] op_sel_hi:[1,0]
	v_exp_f32_e32 v128, v128
	v_exp_f32_e32 v129, v129
	v_exp_f32_e32 v130, v130
	v_exp_f32_e32 v131, v131
	v_exp_f32_e32 v120, v120
	v_exp_f32_e32 v121, v121
	v_exp_f32_e32 v122, v122
	v_exp_f32_e32 v123, v123
	v_pk_add_f32 v[128:129], v[128:129], 1.0 op_sel_hi:[1,0]
	v_pk_add_f32 v[130:131], v[130:131], 1.0 op_sel_hi:[1,0]
	v_pk_add_f32 v[120:121], v[120:121], 1.0 op_sel_hi:[1,0]
	v_pk_add_f32 v[122:123], v[122:123], 1.0 op_sel_hi:[1,0]
	v_rcp_f32_e32 v128, v128
	v_rcp_f32_e32 v129, v129
	v_rcp_f32_e32 v130, v130
	v_rcp_f32_e32 v131, v131
	v_rcp_f32_e32 v120, v120
	v_rcp_f32_e32 v121, v121
	v_rcp_f32_e32 v122, v122
	v_rcp_f32_e32 v123, v123
	v_pk_mul_f32 v[124:125], v[124:125], v[128:129]
	v_pk_mul_f32 v[126:127], v[126:127], v[130:131]
	v_pk_mul_f32 v[116:117], v[116:117], v[120:121]
	v_pk_mul_f32 v[118:119], v[118:119], v[122:123]
	v_pk_mul_f32 v[124:125], v[124:125], 4.0 op_sel_hi:[1,0]
	v_pk_mul_f32 v[126:127], v[126:127], 4.0 op_sel_hi:[1,0]
	v_pk_mul_f32 v[116:117], v[116:117], 4.0 op_sel_hi:[1,0]
	v_pk_mul_f32 v[118:119], v[118:119], 4.0 op_sel_hi:[1,0]
	s_mov_b32 s50, 0x8000
	v_cvt_pk_fp8_f32 v20, v124, v125
	v_cvt_pk_fp8_f32 v21, v116, v117
	v_lshl_add_u64 v[22:23], s[50:51], 0, v[18:19]
	v_cvt_pk_fp8_f32 v20, v126, v127 op_sel:[0,0,1]
	v_cvt_pk_fp8_f32 v21, v118, v119 op_sel:[0,0,1]
	s_nop 0
	global_store_dwordx2 v[22:23], v[20:21], off
	v_pk_fma_f32 v[112:113], v[112:113], v[24:25], v[10:11]
	v_pk_fma_f32 v[114:115], v[114:115], v[24:25], v[12:13]
	v_pk_fma_f32 v[104:105], v[104:105], v[24:25], v[2:3]
; __device__ __forceinline__ unsigned pk4_fp8(float a, float b, float c, float d) { int r = __builtin_amdgcn_cvt_pk_fp8_f32(a, b, 0, false); return (unsigned)__builtin_amdgcn_cvt_pk_fp8_f32(c, d, r, true); }
;     __device__ __forceinline__ void operator()(const f32x4 (&acc)[2][2][4][2], const Unit& u, int wr, int wc, int fr, int fq) const {
;     ...
;                 for (int n = 0; n < 2; ++n)
; #pragma unroll
;                     for (int j = 0; j < 4; ++j) { float g = acc[ai][0][m][n][j] * ws + gb[n][j], up = acc[ai][1][m][n][j] * ws + ub[n][j];
;                         g = fminf(g, 7.f); up = fminf(fmaxf(up, -7.f), 7.f);
;                         hv[n * 4 + j] = (up + 1.f) * g * __builtin_amdgcn_rcpf(1.f + __expf(-1.702f * g)); }
;                 *(u32x2*)rowp = (u32x2){pk4_fp8(4.f * hv[0], 4.f * hv[1], 4.f * hv[2], 4.f * hv[3]), pk4_fp8(4.f * hv[4], 4.f * hv[5], 4.f * hv[6], 4.f * hv[7])}; }
	v_pk_fma_f32 v[106:107], v[106:107], v[24:25], v[4:5]
	v_pk_fma_f32 v[108:109], v[108:109], v[24:25], v[14:15]
	v_pk_fma_f32 v[110:111], v[110:111], v[24:25], v[16:17]
	v_pk_fma_f32 v[100:101], v[100:101], v[24:25], v[6:7]
	v_pk_fma_f32 v[102:103], v[102:103], v[24:25], v[8:9]
	v_min_f32_e32 v112, 0x40e00000, v112
	v_min_f32_e32 v113, 0x40e00000, v113
	v_min_f32_e32 v114, 0x40e00000, v114
	v_min_f32_e32 v115, 0x40e00000, v115
	v_min_f32_e32 v104, 0x40e00000, v104
	v_min_f32_e32 v105, 0x40e00000, v105
	v_min_f32_e32 v106, 0x40e00000, v106
	v_min_f32_e32 v107, 0x40e00000, v107
	v_med3_f32 v108, v108, s35, v200
	v_med3_f32 v109, v109, s35, v200
	v_med3_f32 v110, v110, s35, v200
	v_med3_f32 v111, v111, s35, v200
	v_med3_f32 v100, v100, s35, v200
	v_med3_f32 v101, v101, s35, v200
	v_med3_f32 v102, v102, s35, v200
	v_med3_f32 v103, v103, s35, v200
	v_pk_add_f32 v[108:109], v[108:109], 1.0 op_sel_hi:[1,0]
	v_pk_add_f32 v[110:111], v[110:111], 1.0 op_sel_hi:[1,0]
	v_pk_add_f32 v[100:101], v[100:101], 1.0 op_sel_hi:[1,0]
	v_pk_add_f32 v[102:103], v[102:103], 1.0 op_sel_hi:[1,0]
	v_pk_mul_f32 v[108:109], v[112:113], v[108:109]
	v_pk_mul_f32 v[110:111], v[114:115], v[110:111]
	v_pk_mul_f32 v[100:101], v[104:105], v[100:101]
	v_pk_mul_f32 v[102:103], v[106:107], v[102:103]
	v_pk_mul_f32 v[112:113], v[112:113], v[26:27]
	v_pk_mul_f32 v[114:115], v[114:115], v[26:27]
	v_pk_mul_f32 v[104:105], v[104:105], v[26:27]
	v_pk_mul_f32 v[106:107], v[106:107], v[26:27]
	v_pk_mul_f32 v[112:113], v[112:113], v[196:197] op_sel_hi:[1,0]
	v_pk_mul_f32 v[114:115], v[114:115], v[196:197] op_sel_hi:[1,0]
	v_pk_mul_f32 v[104:105], v[104:105], v[196:197] op_sel_hi:[1,0]
	v_pk_mul_f32 v[106:107], v[106:107], v[196:197] op_sel_hi:[1,0]
	v_exp_f32_e32 v112, v112
	v_exp_f32_e32 v113, v113
	v_exp_f32_e32 v114, v114
	v_exp_f32_e32 v115, v115
	v_exp_f32_e32 v104, v104
	v_exp_f32_e32 v105, v105
	v_exp_f32_e32 v106, v106
	v_exp_f32_e32 v107, v107
	v_pk_add_f32 v[112:113], v[112:113], 1.0 op_sel_hi:[1,0]
	v_pk_add_f32 v[114:115], v[114:115], 1.0 op_sel_hi:[1,0]
	v_pk_add_f32 v[104:105], v[104:105], 1.0 op_sel_hi:[1,0]
	v_pk_add_f32 v[106:107], v[106:107], 1.0 op_sel_hi:[1,0]
	v_rcp_f32_e32 v112, v112
	v_rcp_f32_e32 v113, v113
	v_rcp_f32_e32 v114, v114
	v_rcp_f32_e32 v115, v115
	v_rcp_f32_e32 v104, v104
	v_rcp_f32_e32 v105, v105
	v_rcp_f32_e32 v106, v106
	v_rcp_f32_e32 v107, v107
	v_pk_mul_f32 v[108:109], v[108:109], v[112:113]
	v_pk_mul_f32 v[110:111], v[110:111], v[114:115]
	v_pk_mul_f32 v[100:101], v[100:101], v[104:105]
	v_pk_mul_f32 v[102:103], v[102:103], v[106:107]
	v_pk_mul_f32 v[108:109], v[108:109], 4.0 op_sel_hi:[1,0]
	v_pk_mul_f32 v[110:111], v[110:111], 4.0 op_sel_hi:[1,0]
	v_pk_mul_f32 v[100:101], v[100:101], 4.0 op_sel_hi:[1,0]
	v_pk_mul_f32 v[102:103], v[102:103], 4.0 op_sel_hi:[1,0]
	s_mov_b32 s50, 0xc000
	v_cvt_pk_fp8_f32 v20, v108, v109
	v_cvt_pk_fp8_f32 v21, v100, v101
	v_lshl_add_u64 v[22:23], s[50:51], 0, v[18:19]
	v_cvt_pk_fp8_f32 v20, v110, v111 op_sel:[0,0,1]
	v_cvt_pk_fp8_f32 v21, v102, v103 op_sel:[0,0,1]
	s_nop 0
	global_store_dwordx2 v[22:23], v[20:21], off
	v_pk_fma_f32 v[96:97], v[96:97], v[24:25], v[10:11]
	v_pk_fma_f32 v[98:99], v[98:99], v[24:25], v[12:13]
	v_pk_fma_f32 v[88:89], v[88:89], v[24:25], v[2:3]
	v_pk_fma_f32 v[90:91], v[90:91], v[24:25], v[4:5]
	v_pk_fma_f32 v[92:93], v[92:93], v[24:25], v[14:15]
	v_pk_fma_f32 v[94:95], v[94:95], v[24:25], v[16:17]
	v_pk_fma_f32 v[84:85], v[84:85], v[24:25], v[6:7]
	v_pk_fma_f32 v[86:87], v[86:87], v[24:25], v[8:9]
	v_min_f32_e32 v96, 0x40e00000, v96
	v_min_f32_e32 v97, 0x40e00000, v97
	v_min_f32_e32 v98, 0x40e00000, v98
	v_min_f32_e32 v99, 0x40e00000, v99
	v_min_f32_e32 v88, 0x40e00000, v88
	v_min_f32_e32 v89, 0x40e00000, v89
	v_min_f32_e32 v90, 0x40e00000, v90
	v_min_f32_e32 v91, 0x40e00000, v91
	v_med3_f32 v92, v92, s35, v200
	v_med3_f32 v93, v93, s35, v200
	v_med3_f32 v94, v94, s35, v200
	v_med3_f32 v95, v95, s35, v200
	v_med3_f32 v84, v84, s35, v200
	v_med3_f32 v85, v85, s35, v200
	v_med3_f32 v86, v86, s35, v200
	v_med3_f32 v87, v87, s35, v200
	v_pk_add_f32 v[92:93], v[92:93], 1.0 op_sel_hi:[1,0]
	v_pk_add_f32 v[94:95], v[94:95], 1.0 op_sel_hi:[1,0]
	v_pk_add_f32 v[84:85], v[84:85], 1.0 op_sel_hi:[1,0]
	v_pk_add_f32 v[86:87], v[86:87], 1.0 op_sel_hi:[1,0]
	v_pk_mul_f32 v[92:93], v[96:97], v[92:93]
	v_pk_mul_f32 v[94:95], v[98:99], v[94:95]
	v_pk_mul_f32 v[84:85], v[88:89], v[84:85]
	v_pk_mul_f32 v[86:87], v[90:91], v[86:87]
	v_pk_mul_f32 v[96:97], v[96:97], v[26:27]
	v_pk_mul_f32 v[98:99], v[98:99], v[26:27]
	v_pk_mul_f32 v[88:89], v[88:89], v[26:27]
	v_pk_mul_f32 v[90:91], v[90:91], v[26:27]
	v_pk_mul_f32 v[96:97], v[96:97], v[196:197] op_sel_hi:[1,0]
	v_pk_mul_f32 v[98:99], v[98:99], v[196:197] op_sel_hi:[1,0]
	v_pk_mul_f32 v[88:89], v[88:89], v[196:197] op_sel_hi:[1,0]
	v_pk_mul_f32 v[90:91], v[90:91], v[196:197] op_sel_hi:[1,0]
	v_exp_f32_e32 v96, v96
	v_exp_f32_e32 v97, v97
	v_exp_f32_e32 v98, v98
	v_exp_f32_e32 v99, v99
	v_exp_f32_e32 v88, v88
	v_exp_f32_e32 v89, v89
	v_exp_f32_e32 v90, v90
	v_exp_f32_e32 v91, v91
	v_pk_add_f32 v[96:97], v[96:97], 1.0 op_sel_hi:[1,0]
	v_pk_add_f32 v[98:99], v[98:99], 1.0 op_sel_hi:[1,0]
	v_pk_add_f32 v[88:89], v[88:89], 1.0 op_sel_hi:[1,0]
	v_pk_add_f32 v[90:91], v[90:91], 1.0 op_sel_hi:[1,0]
	v_rcp_f32_e32 v96, v96
	v_rcp_f32_e32 v97, v97
	v_rcp_f32_e32 v98, v98
	v_rcp_f32_e32 v99, v99
	v_rcp_f32_e32 v88, v88
	v_rcp_f32_e32 v89, v89
	v_rcp_f32_e32 v90, v90
	v_rcp_f32_e32 v91, v91
	v_pk_mul_f32 v[92:93], v[92:93], v[96:97]
	v_pk_mul_f32 v[94:95], v[94:95], v[98:99]
	v_pk_mul_f32 v[84:85], v[84:85], v[88:89]
	v_pk_mul_f32 v[86:87], v[86:87], v[90:91]
; __device__ __forceinline__ unsigned pk4_fp8(float a, float b, float c, float d) { int r = __builtin_amdgcn_cvt_pk_fp8_f32(a, b, 0, false); return (unsigned)__builtin_amdgcn_cvt_pk_fp8_f32(c, d, r, true); }
;     __device__ __forceinline__ void operator()(const f32x4 (&acc)[2][2][4][2], const Unit& u, int wr, int wc, int fr, int fq) const {
;     ...
;             for (int m = 0; m < 4; ++m) { unsigned char* rowp = (unsigned char*)H + (size_t)(r0 + ai * HALF + m * 16) * 1024 + j0; float hv[8];
; #pragma unroll
;                 for (int n = 0; n < 2; ++n)
; #pragma unroll
;                     for (int j = 0; j < 4; ++j) { float g = acc[ai][0][m][n][j] * ws + gb[n][j], up = acc[ai][1][m][n][j] * ws + ub[n][j];
;                         g = fminf(g, 7.f); up = fminf(fmaxf(up, -7.f), 7.f);
;                         hv[n * 4 + j] = (up + 1.f) * g * __builtin_amdgcn_rcpf(1.f + __expf(-1.702f * g)); }
;                 *(u32x2*)rowp = (u32x2){pk4_fp8(4.f * hv[0], 4.f * hv[1], 4.f * hv[2], 4.f * hv[3]), pk4_fp8(4.f * hv[4], 4.f * hv[5], 4.f * hv[6], 4.f * hv[7])}; }
	v_pk_mul_f32 v[92:93], v[92:93], 4.0 op_sel_hi:[1,0]
	v_pk_mul_f32 v[94:95], v[94:95], 4.0 op_sel_hi:[1,0]
	v_pk_mul_f32 v[84:85], v[84:85], 4.0 op_sel_hi:[1,0]
	v_pk_mul_f32 v[86:87], v[86:87], 4.0 op_sel_hi:[1,0]
	s_mov_b32 s50, 0x20000
	v_cvt_pk_fp8_f32 v20, v92, v93
	v_cvt_pk_fp8_f32 v21, v84, v85
	v_lshl_add_u64 v[22:23], s[50:51], 0, v[18:19]
	v_cvt_pk_fp8_f32 v20, v94, v95 op_sel:[0,0,1]
	v_cvt_pk_fp8_f32 v21, v86, v87 op_sel:[0,0,1]
	s_nop 0
	global_store_dwordx2 v[22:23], v[20:21], off
	v_pk_fma_f32 v[80:81], v[80:81], v[24:25], v[10:11]
	v_pk_fma_f32 v[82:83], v[82:83], v[24:25], v[12:13]
	v_pk_fma_f32 v[72:73], v[72:73], v[24:25], v[2:3]
	v_pk_fma_f32 v[74:75], v[74:75], v[24:25], v[4:5]
	v_pk_fma_f32 v[76:77], v[76:77], v[24:25], v[14:15]
	v_pk_fma_f32 v[78:79], v[78:79], v[24:25], v[16:17]
	v_pk_fma_f32 v[68:69], v[68:69], v[24:25], v[6:7]
	v_pk_fma_f32 v[70:71], v[70:71], v[24:25], v[8:9]
	v_min_f32_e32 v80, 0x40e00000, v80
	v_min_f32_e32 v81, 0x40e00000, v81
	v_min_f32_e32 v82, 0x40e00000, v82
	v_min_f32_e32 v83, 0x40e00000, v83
	v_min_f32_e32 v72, 0x40e00000, v72
	v_min_f32_e32 v73, 0x40e00000, v73
	v_min_f32_e32 v74, 0x40e00000, v74
	v_min_f32_e32 v75, 0x40e00000, v75
	v_med3_f32 v76, v76, s35, v200
	v_med3_f32 v77, v77, s35, v200
	v_med3_f32 v78, v78, s35, v200
	v_med3_f32 v79, v79, s35, v200
	v_med3_f32 v68, v68, s35, v200
	v_med3_f32 v69, v69, s35, v200
	v_med3_f32 v70, v70, s35, v200
	v_med3_f32 v71, v71, s35, v200
	v_pk_add_f32 v[76:77], v[76:77], 1.0 op_sel_hi:[1,0]
	v_pk_add_f32 v[78:79], v[78:79], 1.0 op_sel_hi:[1,0]
	v_pk_add_f32 v[68:69], v[68:69], 1.0 op_sel_hi:[1,0]
	v_pk_add_f32 v[70:71], v[70:71], 1.0 op_sel_hi:[1,0]
	v_pk_mul_f32 v[76:77], v[80:81], v[76:77]
	v_pk_mul_f32 v[78:79], v[82:83], v[78:79]
	v_pk_mul_f32 v[68:69], v[72:73], v[68:69]
	v_pk_mul_f32 v[70:71], v[74:75], v[70:71]
	v_pk_mul_f32 v[80:81], v[80:81], v[26:27]
	v_pk_mul_f32 v[82:83], v[82:83], v[26:27]
	v_pk_mul_f32 v[72:73], v[72:73], v[26:27]
	v_pk_mul_f32 v[74:75], v[74:75], v[26:27]
	v_pk_mul_f32 v[80:81], v[80:81], v[196:197] op_sel_hi:[1,0]
	v_pk_mul_f32 v[82:83], v[82:83], v[196:197] op_sel_hi:[1,0]
	v_pk_mul_f32 v[72:73], v[72:73], v[196:197] op_sel_hi:[1,0]
	v_pk_mul_f32 v[74:75], v[74:75], v[196:197] op_sel_hi:[1,0]
	v_exp_f32_e32 v80, v80
	v_exp_f32_e32 v81, v81
	v_exp_f32_e32 v82, v82
	v_exp_f32_e32 v83, v83
	v_exp_f32_e32 v72, v72
	v_exp_f32_e32 v73, v73
	v_exp_f32_e32 v74, v74
	v_exp_f32_e32 v75, v75
	v_pk_add_f32 v[80:81], v[80:81], 1.0 op_sel_hi:[1,0]
	v_pk_add_f32 v[82:83], v[82:83], 1.0 op_sel_hi:[1,0]
	v_pk_add_f32 v[72:73], v[72:73], 1.0 op_sel_hi:[1,0]
	v_pk_add_f32 v[74:75], v[74:75], 1.0 op_sel_hi:[1,0]
	v_rcp_f32_e32 v80, v80
	v_rcp_f32_e32 v81, v81
	v_rcp_f32_e32 v82, v82
	v_rcp_f32_e32 v83, v83
	v_rcp_f32_e32 v72, v72
	v_rcp_f32_e32 v73, v73
	v_rcp_f32_e32 v74, v74
	v_rcp_f32_e32 v75, v75
	v_pk_mul_f32 v[76:77], v[76:77], v[80:81]
	v_pk_mul_f32 v[78:79], v[78:79], v[82:83]
	v_pk_mul_f32 v[68:69], v[68:69], v[72:73]
	v_pk_mul_f32 v[70:71], v[70:71], v[74:75]
	v_pk_mul_f32 v[76:77], v[76:77], 4.0 op_sel_hi:[1,0]
	v_pk_mul_f32 v[78:79], v[78:79], 4.0 op_sel_hi:[1,0]
	v_pk_mul_f32 v[68:69], v[68:69], 4.0 op_sel_hi:[1,0]
	v_pk_mul_f32 v[70:71], v[70:71], 4.0 op_sel_hi:[1,0]
	s_mov_b32 s50, 0x24000
	v_cvt_pk_fp8_f32 v20, v76, v77
	v_cvt_pk_fp8_f32 v21, v68, v69
	v_lshl_add_u64 v[22:23], s[50:51], 0, v[18:19]
	v_cvt_pk_fp8_f32 v20, v78, v79 op_sel:[0,0,1]
	v_cvt_pk_fp8_f32 v21, v70, v71 op_sel:[0,0,1]
	s_nop 0
	global_store_dwordx2 v[22:23], v[20:21], off
	v_pk_fma_f32 v[60:61], v[60:61], v[24:25], v[10:11]
	v_pk_fma_f32 v[62:63], v[62:63], v[24:25], v[12:13]
	v_pk_fma_f32 v[52:53], v[52:53], v[24:25], v[2:3]
	v_pk_fma_f32 v[54:55], v[54:55], v[24:25], v[4:5]
	v_pk_fma_f32 v[64:65], v[64:65], v[24:25], v[14:15]
	v_pk_fma_f32 v[66:67], v[66:67], v[24:25], v[16:17]
	v_pk_fma_f32 v[56:57], v[56:57], v[24:25], v[6:7]
	v_pk_fma_f32 v[58:59], v[58:59], v[24:25], v[8:9]
	v_min_f32_e32 v60, 0x40e00000, v60
	v_min_f32_e32 v61, 0x40e00000, v61
	v_min_f32_e32 v62, 0x40e00000, v62
	v_min_f32_e32 v63, 0x40e00000, v63
	v_min_f32_e32 v52, 0x40e00000, v52
	v_min_f32_e32 v53, 0x40e00000, v53
	v_min_f32_e32 v54, 0x40e00000, v54
	v_min_f32_e32 v55, 0x40e00000, v55
	v_med3_f32 v64, v64, s35, v200
	v_med3_f32 v65, v65, s35, v200
	v_med3_f32 v66, v66, s35, v200
	v_med3_f32 v67, v67, s35, v200
	v_med3_f32 v56, v56, s35, v200
	v_med3_f32 v57, v57, s35, v200
	v_med3_f32 v58, v58, s35, v200
	v_med3_f32 v59, v59, s35, v200
	v_pk_add_f32 v[64:65], v[64:65], 1.0 op_sel_hi:[1,0]
	v_pk_add_f32 v[66:67], v[66:67], 1.0 op_sel_hi:[1,0]
	v_pk_add_f32 v[56:57], v[56:57], 1.0 op_sel_hi:[1,0]
	v_pk_add_f32 v[58:59], v[58:59], 1.0 op_sel_hi:[1,0]
	v_pk_mul_f32 v[64:65], v[60:61], v[64:65]
	v_pk_mul_f32 v[66:67], v[62:63], v[66:67]
	v_pk_mul_f32 v[56:57], v[52:53], v[56:57]
	v_pk_mul_f32 v[58:59], v[54:55], v[58:59]
; __device__ __forceinline__ unsigned pk4_fp8(float a, float b, float c, float d) { int r = __builtin_amdgcn_cvt_pk_fp8_f32(a, b, 0, false); return (unsigned)__builtin_amdgcn_cvt_pk_fp8_f32(c, d, r, true); }
;     __device__ __forceinline__ void operator()(const f32x4 (&acc)[2][2][4][2], const Unit& u, int wr, int wc, int fr, int fq) const {
;     ...
;             for (int m = 0; m < 4; ++m) { unsigned char* rowp = (unsigned char*)H + (size_t)(r0 + ai * HALF + m * 16) * 1024 + j0; float hv[8];
; #pragma unroll
;                 for (int n = 0; n < 2; ++n)
; #pragma unroll
;                     for (int j = 0; j < 4; ++j) { float g = acc[ai][0][m][n][j] * ws + gb[n][j], up = acc[ai][1][m][n][j] * ws + ub[n][j];
;                         g = fminf(g, 7.f); up = fminf(fmaxf(up, -7.f), 7.f);
;                         hv[n * 4 + j] = (up + 1.f) * g * __builtin_amdgcn_rcpf(1.f + __expf(-1.702f * g)); }
;                 *(u32x2*)rowp = (u32x2){pk4_fp8(4.f * hv[0], 4.f * hv[1], 4.f * hv[2], 4.f * hv[3]), pk4_fp8(4.f * hv[4], 4.f * hv[5], 4.f * hv[6], 4.f * hv[7])}; }
	v_pk_mul_f32 v[60:61], v[60:61], v[26:27]
	v_pk_mul_f32 v[62:63], v[62:63], v[26:27]
	v_pk_mul_f32 v[52:53], v[52:53], v[26:27]
	v_pk_mul_f32 v[54:55], v[54:55], v[26:27]
	v_pk_mul_f32 v[60:61], v[60:61], v[196:197] op_sel_hi:[1,0]
	v_pk_mul_f32 v[62:63], v[62:63], v[196:197] op_sel_hi:[1,0]
	v_pk_mul_f32 v[52:53], v[52:53], v[196:197] op_sel_hi:[1,0]
	v_pk_mul_f32 v[54:55], v[54:55], v[196:197] op_sel_hi:[1,0]
	v_exp_f32_e32 v60, v60
	v_exp_f32_e32 v61, v61
	v_exp_f32_e32 v62, v62
	v_exp_f32_e32 v63, v63
	v_exp_f32_e32 v52, v52
	v_exp_f32_e32 v53, v53
	v_exp_f32_e32 v54, v54
	v_exp_f32_e32 v55, v55
	v_pk_add_f32 v[60:61], v[60:61], 1.0 op_sel_hi:[1,0]
	v_pk_add_f32 v[62:63], v[62:63], 1.0 op_sel_hi:[1,0]
	v_pk_add_f32 v[52:53], v[52:53], 1.0 op_sel_hi:[1,0]
	v_pk_add_f32 v[54:55], v[54:55], 1.0 op_sel_hi:[1,0]
	v_rcp_f32_e32 v60, v60
	v_rcp_f32_e32 v61, v61
	v_rcp_f32_e32 v62, v62
	v_rcp_f32_e32 v63, v63
	v_rcp_f32_e32 v52, v52
	v_rcp_f32_e32 v53, v53
	v_rcp_f32_e32 v54, v54
	v_rcp_f32_e32 v55, v55
	v_pk_mul_f32 v[64:65], v[64:65], v[60:61]
	v_pk_mul_f32 v[66:67], v[66:67], v[62:63]
	v_pk_mul_f32 v[56:57], v[56:57], v[52:53]
	v_pk_mul_f32 v[58:59], v[58:59], v[54:55]
	v_pk_mul_f32 v[64:65], v[64:65], 4.0 op_sel_hi:[1,0]
	v_pk_mul_f32 v[66:67], v[66:67], 4.0 op_sel_hi:[1,0]
	v_pk_mul_f32 v[56:57], v[56:57], 4.0 op_sel_hi:[1,0]
	v_pk_mul_f32 v[58:59], v[58:59], 4.0 op_sel_hi:[1,0]
	s_mov_b32 s50, 0x28000
	v_cvt_pk_fp8_f32 v20, v64, v65
	v_cvt_pk_fp8_f32 v21, v56, v57
	v_lshl_add_u64 v[22:23], s[50:51], 0, v[18:19]
	v_cvt_pk_fp8_f32 v20, v66, v67 op_sel:[0,0,1]
	v_cvt_pk_fp8_f32 v21, v58, v59 op_sel:[0,0,1]
	s_nop 0
	global_store_dwordx2 v[22:23], v[20:21], off
	v_pk_fma_f32 v[44:45], v[44:45], v[24:25], v[10:11]
	v_pk_fma_f32 v[46:47], v[46:47], v[24:25], v[12:13]
	v_pk_fma_f32 v[36:37], v[36:37], v[24:25], v[2:3]
	v_pk_fma_f32 v[38:39], v[38:39], v[24:25], v[4:5]
	v_pk_fma_f32 v[48:49], v[48:49], v[24:25], v[14:15]
	v_pk_fma_f32 v[50:51], v[50:51], v[24:25], v[16:17]
	v_pk_fma_f32 v[40:41], v[40:41], v[24:25], v[6:7]
	v_pk_fma_f32 v[42:43], v[42:43], v[24:25], v[8:9]
	v_min_f32_e32 v44, 0x40e00000, v44
	v_min_f32_e32 v45, 0x40e00000, v45
	v_min_f32_e32 v46, 0x40e00000, v46
	v_min_f32_e32 v47, 0x40e00000, v47
	v_min_f32_e32 v36, 0x40e00000, v36
	v_min_f32_e32 v37, 0x40e00000, v37
	v_min_f32_e32 v38, 0x40e00000, v38
	v_min_f32_e32 v39, 0x40e00000, v39
	v_med3_f32 v48, v48, s35, v200
	v_med3_f32 v49, v49, s35, v200
	v_med3_f32 v50, v50, s35, v200
	v_med3_f32 v51, v51, s35, v200
	v_med3_f32 v40, v40, s35, v200
	v_med3_f32 v41, v41, s35, v200
	v_med3_f32 v42, v42, s35, v200
	v_med3_f32 v43, v43, s35, v200
	v_pk_add_f32 v[48:49], v[48:49], 1.0 op_sel_hi:[1,0]
	v_pk_add_f32 v[50:51], v[50:51], 1.0 op_sel_hi:[1,0]
	v_pk_add_f32 v[40:41], v[40:41], 1.0 op_sel_hi:[1,0]
	v_pk_add_f32 v[42:43], v[42:43], 1.0 op_sel_hi:[1,0]
	v_pk_mul_f32 v[48:49], v[44:45], v[48:49]
	v_pk_mul_f32 v[50:51], v[46:47], v[50:51]
	v_pk_mul_f32 v[40:41], v[36:37], v[40:41]
	v_pk_mul_f32 v[42:43], v[38:39], v[42:43]
	v_pk_mul_f32 v[44:45], v[44:45], v[26:27]
	v_pk_mul_f32 v[46:47], v[46:47], v[26:27]
	v_pk_mul_f32 v[36:37], v[36:37], v[26:27]
	v_pk_mul_f32 v[38:39], v[38:39], v[26:27]
	v_pk_mul_f32 v[44:45], v[44:45], v[196:197] op_sel_hi:[1,0]
	v_pk_mul_f32 v[46:47], v[46:47], v[196:197] op_sel_hi:[1,0]
	v_pk_mul_f32 v[36:37], v[36:37], v[196:197] op_sel_hi:[1,0]
	v_pk_mul_f32 v[38:39], v[38:39], v[196:197] op_sel_hi:[1,0]
	v_exp_f32_e32 v44, v44
	v_exp_f32_e32 v45, v45
	v_exp_f32_e32 v46, v46
	v_exp_f32_e32 v47, v47
	v_exp_f32_e32 v36, v36
	v_exp_f32_e32 v37, v37
	v_exp_f32_e32 v38, v38
	v_exp_f32_e32 v39, v39
	v_pk_add_f32 v[44:45], v[44:45], 1.0 op_sel_hi:[1,0]
	v_pk_add_f32 v[46:47], v[46:47], 1.0 op_sel_hi:[1,0]
	v_pk_add_f32 v[36:37], v[36:37], 1.0 op_sel_hi:[1,0]
	v_pk_add_f32 v[38:39], v[38:39], 1.0 op_sel_hi:[1,0]
	v_rcp_f32_e32 v44, v44
	v_rcp_f32_e32 v45, v45
	v_rcp_f32_e32 v46, v46
	v_rcp_f32_e32 v47, v47
	v_rcp_f32_e32 v36, v36
	v_rcp_f32_e32 v37, v37
	v_rcp_f32_e32 v38, v38
	v_rcp_f32_e32 v39, v39
	v_pk_mul_f32 v[48:49], v[48:49], v[44:45]
	v_pk_mul_f32 v[50:51], v[50:51], v[46:47]
	v_pk_mul_f32 v[40:41], v[40:41], v[36:37]
	v_pk_mul_f32 v[42:43], v[42:43], v[38:39]
	v_pk_mul_f32 v[48:49], v[48:49], 4.0 op_sel_hi:[1,0]
	v_pk_mul_f32 v[50:51], v[50:51], 4.0 op_sel_hi:[1,0]
	v_pk_mul_f32 v[40:41], v[40:41], 4.0 op_sel_hi:[1,0]
	v_pk_mul_f32 v[42:43], v[42:43], 4.0 op_sel_hi:[1,0]
	s_mov_b32 s50, 0x2c000
	v_cvt_pk_fp8_f32 v20, v48, v49
	v_cvt_pk_fp8_f32 v21, v40, v41
	v_lshl_add_u64 v[22:23], s[50:51], 0, v[18:19]
	v_cvt_pk_fp8_f32 v20, v50, v51 op_sel:[0,0,1]
	v_cvt_pk_fp8_f32 v21, v42, v43 op_sel:[0,0,1]
	s_nop 0
	global_store_dwordx2 v[22:23], v[20:21], off
	s_and_b64 vcc, exec, s[38:39]
	s_cbranch_vccnz .LBB0_3128
	s_andn2_b64 vcc, exec, s[6:7]
	s_cbranch_vccnz .LBB0_3127
	s_barrier
	s_branch .LBB0_3127

;     __device__ __forceinline__ bool next(int i, Unit& u) const {
;         const int L = i * G + c; if (L >= total) return false;
;         int e = 0;
; #pragma unroll 1
;         for (int j = 1; j < NEXP; ++j) e = (L >= pre[j]) ? j : e;
;         const int rem = L - pre[e];
;         u.e = e; u.pn = rem % NT; u.mt = rem / NT; u.pm = 0; return true;
;     }
.LBB0_3223:
	s_add_i32 s23, s23, 1
	s_mul_i32 s15, s23, s68
	v_readlane_b32 s27, v250, 39
	s_add_i32 s15, s15, s27
	v_cmp_ge_i32_e32 vcc, s15, v1
	v_cmp_lt_i32_e64 s[40:41], s15, v1
	s_cbranch_vccnz .LBB0_3229
	v_lshl_add_u32 v2, v195, 2, 0
	v_add_u32_e32 v2, 0x23100, v2
	ds_read_b32 v2, v2
	s_waitcnt lgkmcnt(0)
	v_cmp_ge_i32_e32 vcc, s15, v2
	s_and_b32 s14, vcc_lo, -2
	s_bcnt1_i32_b32 s14, s14
	s_nop 3
	v_readlane_b32 s26, v2, s14
	s_sub_i32 s15, s15, s26
	s_ashr_i32 s26, s15, 31
	s_lshr_b32 s26, s26, 30
	s_add_i32 s26, s15, s26
	s_ashr_i32 s36, s26, 2
	s_and_b32 s26, s26, -4
	s_sub_i32 s26, s15, s26
